# P2: fixed contiguous unit range per logical XCD (no slice rotation across rounds), A panels reused across rounds in L2
# baseline (speedup 1.0000x reference)
.LBB0_267:
	s_cmpk_gt_i32 s20, 0x6ff
	v_readfirstlane_b32 s10, v0
	s_cbranch_scc1 .LBB0_289
	s_add_u32 s16, s76, 0x8687b000
	s_addc_u32 s17, s77, 0
	s_add_u32 s18, s76, 0x6c00
	s_addc_u32 s19, s77, 0
	s_ashr_i32 s21, s20, 31
	s_and_b32 s0, s20, 7
	s_lshr_b32 s1, s20, 3
	s_mul_i32 s4, s0, 231
	s_mul_i32 s6, s0, 220
	s_sub_i32 s6, s6, 198
	s_cmp_lt_u32 s0, 2
	s_cselect_b32 s4, s4, s6
	s_cmp_eq_u32 s0, 2
	s_cselect_b32 s4, 0x61a, s4
	s_add_i32 s0, s4, s1
	s_mul_hi_i32 s1, s0, 0x92492493
	s_add_i32 s1, s1, s0
	s_lshr_b32 s4, s1, 31
	s_ashr_i32 s1, s1, 6
	s_add_i32 s4, s1, s4
	s_lshl_b32 s1, s4, 2
	s_mul_i32 s4, s4, 112
	s_sub_i32 s0, s0, s4
	s_bfe_u32 s4, s0, 0x10007
	s_add_i32 s4, s0, s4
	s_bfe_i32 s6, s4, 0x80000
	s_sext_i32_i16 s12, s6
	s_and_b32 s4, s4, 0xfc
	s_sub_i32 s0, s0, s4
	s_ashr_i32 s74, s12, 2
	s_cmpk_lt_u32 s10, 0x100
	s_sext_i32_i8 s11, s0
	s_cselect_b64 s[6:7], -1, 0
	s_and_b32 s0, s10, 0xffffffc0
	s_mov_b32 s5, 0
	s_cmpk_gt_u32 s10, 0xff
	s_mov_b64 s[8:9], -1
	s_cbranch_scc0 .LBB0_270
	s_lshl_b32 s8, s74, 8
	s_ashr_i32 s9, s8, 31
	s_lshl_b64 s[8:9], s[8:9], 2
	s_add_u32 s13, s18, s8
	s_addc_u32 s14, s19, s9
	s_add_i32 s4, s0, 0xffffff00
	s_lshl_b64 s[8:9], s[4:5], 2
	s_add_u32 s8, s13, s8
	s_addc_u32 s9, s14, s9
	s_lshl_b32 s4, s4, 2
	s_add_i32 s4, s4, 0
	s_waitcnt vmcnt(6)
	v_lshlrev_b32_e32 v2, 2, v190
	s_add_i32 m0, s4, 0x20800
	s_nop 0
	global_load_lds_dword v2, s[8:9]
	s_mov_b64 s[8:9], 0

.LBB0_277:
	s_add_i32 s73, s15, 1
	s_mul_i32 s0, s73, s67
	s_mul_hi_u32 s1, s73, s24
	s_add_i32 s1, s1, s0
	s_mul_i32 s0, s73, s24
	s_add_u32 s4, s0, s20
	s_addc_u32 s5, s1, s21
	v_cmp_gt_i64_e32 vcc, s[4:5], v[150:151]
	v_cmp_lt_i64_e64 s[0:1], s[4:5], v[148:149]
	s_cbranch_vccnz .LBB0_279
	s_and_b32 s5, s20, 7
	s_mul_i32 s4, s5, 231
	s_mul_i32 s16, s5, 220
	s_sub_i32 s16, s16, 198
	s_cmp_lt_u32 s5, 2
	s_cselect_b32 s4, s4, s16
	s_cmp_eq_u32 s5, 2
	s_cselect_b32 s4, 0x61a, s4
	s_cmp_lt_u32 s5, 3
	s_cselect_b32 s16, 21, 20
	s_mul_i32 s16, s16, s73
	s_add_i32 s4, s4, s16
	s_lshr_b32 s16, s20, 3
	s_add_i32 s4, s4, s16
	s_mul_hi_i32 s5, s4, 0x92492493
	s_add_i32 s5, s5, s4
	s_lshr_b32 s16, s5, 31
	s_ashr_i32 s5, s5, 6
	s_add_i32 s5, s5, s16
	s_lshl_b32 s17, s5, 2
	s_sub_i32 s16, 64, s17
	s_min_i32 s18, s16, 4
	s_abs_i32 s16, s18
	v_cvt_f32_u32_e32 v2, s16
	s_sub_i32 s22, 0, s16
	s_mul_i32 s5, s5, 112
	s_sub_i32 s4, s4, s5
	v_rcp_iflag_f32_e32 v2, v2
	s_abs_i32 s5, s4
	s_xor_b32 s19, s4, s18
	s_ashr_i32 s19, s19, 31
	v_mul_f32_e32 v2, 0x4f7ffffe, v2
	v_cvt_u32_f32_e32 v2, v2
	s_nop 0
	v_readfirstlane_b32 s23, v2
	s_mul_i32 s22, s22, s23
	s_mul_hi_u32 s22, s23, s22
	s_add_i32 s23, s23, s22
	s_mul_hi_u32 s22, s5, s23
	s_mul_i32 s23, s22, s16
	s_sub_i32 s5, s5, s23
	s_add_i32 s56, s22, 1
	s_sub_i32 s23, s5, s16
	s_cmp_ge_u32 s5, s16
	s_cselect_b32 s22, s56, s22
	s_cselect_b32 s5, s23, s5
	s_add_i32 s23, s22, 1
	s_cmp_ge_u32 s5, s16
	s_cselect_b32 s5, s23, s22
	s_xor_b32 s5, s5, s19
	s_sub_i32 s16, s5, s19
	s_mul_i32 s5, s16, s18
	s_sub_i32 s4, s4, s5
	s_add_i32 s18, s17, s4
